# baseline (speedup 1.0000x reference)
_Z11proj_kernelPKfS0_S0_PKDF16_S0_S0_S0_PDF16_S3_S3_Pj:
	s_ashr_i32 s12, s2, 6
	s_load_dwordx8 s[4:11], s[0:1], 0x0
	s_cmp_gt_u32 s2, 63
	s_cselect_b64 s[22:23], -1, 0
	s_cmp_lg_u32 s12, 1
	s_cselect_b64 s[18:19], -1, 0
	s_cmp_eq_u32 s12, 1
	s_cselect_b64 s[20:21], -1, 0
	s_and_b64 s[14:15], s[20:21], exec
	s_waitcnt lgkmcnt(0)
	s_cselect_b32 s14, s6, s8
	s_cselect_b32 s15, s7, s9
	s_ashr_i32 s13, s12, 31
	s_lshl_b32 s28, s2, 7
	s_lshl_b64 s[6:7], s[12:13], 19
	s_and_b32 s3, s28, 0x1f80
	s_cmp_lt_u32 s2, 64
	s_cselect_b64 vcc, -1, 0
	v_lshrrev_b32_e32 v1, 2, v0
	v_or_b32_e32 v2, s3, v1
	s_and_b64 s[8:9], vcc, exec
	s_cselect_b32 s25, s5, s15
	s_cselect_b32 s24, s4, s14
	v_lshlrev_b32_e32 v2, 11, v2
	v_mov_b32_e32 v3, 0
	v_lshlrev_b32_e32 v6, 5, v0
	s_add_u32 s4, s10, s6
	v_lshl_add_u64 v[4:5], s[24:25], 0, v[2:3]
	v_and_b32_e32 v6, 0x60, v6
	v_mov_b32_e32 v7, v3
	v_lshlrev_b32_e32 v56, 4, v0
	v_mov_b32_e32 v57, v3
	s_addc_u32 s5, s11, s7
	v_lshl_add_u64 v[4:5], v[4:5], 0, v[6:7]
	s_movk_i32 s8, 0x2000
	v_lshl_add_u64 v[6:7], s[4:5], 0, v[56:57]
	global_load_dwordx4 v[8:11], v[4:5], off sc1 nt
	global_load_dwordx4 v[12:15], v[4:5], off offset:16 sc1 nt
	global_load_dwordx4 v[16:19], v56, s[4:5] sc1
	v_add_co_u32_e64 v28, s[4:5], s8, v6
	s_mov_b32 s33, 0xa000
	s_nop 0
	v_addc_co_u32_e64 v29, s[4:5], 0, v7, s[4:5]
	s_movk_i32 s4, 0x4000
	s_nop 0
	v_add_co_u32_e64 v30, s[4:5], s4, v6
	s_mov_b32 s6, 0xe000
	s_nop 0
	v_addc_co_u32_e64 v31, s[4:5], 0, v7, s[4:5]
	global_load_dwordx4 v[20:23], v[28:29], off sc1
	global_load_dwordx4 v[24:27], v[30:31], off sc1
	s_movk_i32 s4, 0x6000
	v_add_co_u32_e64 v40, s[4:5], s4, v6
	v_lshlrev_b32_e32 v57, 6, v1
	s_nop 0
	v_addc_co_u32_e64 v41, s[4:5], 0, v7, s[4:5]
	global_load_dwordx4 v[28:31], v[40:41], off sc1
	global_load_dwordx4 v[32:35], v[4:5], off offset:128 sc1 nt
	global_load_dwordx4 v[36:39], v[4:5], off offset:144 sc1 nt
	s_mov_b32 s4, 0x8000
	v_add_co_u32_e64 v40, s[4:5], s4, v6
	v_bitop3_b32 v58, v56, 48, v0 bitop3:0x48
	s_nop 0
	v_addc_co_u32_e64 v41, s[4:5], 0, v7, s[4:5]
	v_add_co_u32_e64 v44, s[4:5], s33, v6
	global_load_dwordx4 v[40:43], v[40:41], off sc1
	s_nop 0
	v_addc_co_u32_e64 v45, s[4:5], 0, v7, s[4:5]
	s_mov_b32 s4, 0xc000
	s_nop 0
	v_add_co_u32_e64 v48, s[4:5], s4, v6
	global_load_dwordx4 v[44:47], v[44:45], off sc1
	s_nop 0
	v_addc_co_u32_e64 v49, s[4:5], 0, v7, s[4:5]
	v_add_co_u32_e64 v52, s[4:5], s6, v6
	global_load_dwordx4 v[48:51], v[48:49], off sc1
	s_nop 0
	v_addc_co_u32_e64 v53, s[4:5], 0, v7, s[4:5]
	global_load_dwordx4 v[52:55], v[52:53], off sc1
	s_mov_b32 s4, 0x1e000
	v_add3_u32 v209, 0, v57, v58
	v_add_u32_e32 v208, 0, v56
	v_readfirstlane_b32 s30, v0
	v_bfe_u32 v207, v0, 5, 1
	v_bitop3_b32 v1, v207, v1, 3 bitop3:0x78
	v_lshlrev_b32_e32 v210, 4, v1
	s_mov_b32 s34, 0x14000
	v_add_u32_e32 v213, 0x2000, v208
	s_mov_b32 s43, 0
	s_lshr_b32 s29, s30, 6
	s_mov_b32 s35, -2
	s_mov_b32 s36, 0xffff2000
	s_mov_b32 s37, 0xffff4000
	s_mov_b32 s38, 0xffff6000
	s_movk_i32 s39, 0x8000
	s_movk_i32 s40, 0xa000
	s_movk_i32 s41, 0xc000
	s_movk_i32 s42, 0xe000
	s_mov_b64 s[26:27], 0x100
	v_mov_b32_e32 v56, v3
	v_mov_b32_e32 v57, v3
	v_mov_b32_e32 v58, v3
	v_mov_b32_e32 v59, v3
	v_mov_b32_e32 v60, v3
	v_mov_b32_e32 v61, v3
	v_mov_b32_e32 v62, v3
	v_mov_b32_e32 v63, v3
	v_mov_b32_e32 v64, v3
	v_mov_b32_e32 v65, v3
	v_mov_b32_e32 v66, v3
	v_mov_b32_e32 v67, v3
	v_mov_b32_e32 v68, v3
	v_mov_b32_e32 v69, v3
	v_mov_b32_e32 v70, v3
	s_waitcnt vmcnt(11)
	v_cvt_pk_f16_f32 v8, v8, v9
	v_cvt_pk_f16_f32 v9, v10, v11
	s_waitcnt vmcnt(10)
	v_cvt_pk_f16_f32 v10, v12, v13
	v_cvt_pk_f16_f32 v11, v14, v15
	ds_write_b128 v209, v[8:11]
	v_and_b32_e32 v10, 31, v0
	s_waitcnt vmcnt(9)
	ds_write_b128 v208, v[16:19] offset:8192
	s_waitcnt vmcnt(8)
	ds_write_b128 v208, v[20:23] offset:16384
	s_waitcnt vmcnt(7)
	ds_write_b128 v208, v[24:27] offset:24576
	s_load_dwordx2 s[16:17], s[0:1], 0x50
	s_load_dwordx4 s[12:15], s[0:1], 0x40
	s_load_dwordx8 s[4:11], s[0:1], 0x20
	s_lshl_b32 s0, s30, 1
	s_and_b32 s31, s0, 0x180
	s_lshr_b32 s0, s30, 2
	v_bfe_u32 v11, v0, 2, 2
	s_and_b32 s0, s0, 0x3fffffc0
	s_waitcnt vmcnt(5)
	v_cvt_pk_f16_f32 v8, v32, v33
	v_cvt_pk_f16_f32 v9, v34, v35
	v_or_b32_e32 v12, s31, v10
	v_or_b32_e32 v206, s0, v10
	v_bitop3_b32 v1, v207, v11, 2 bitop3:0x36
	s_waitcnt vmcnt(4)
	v_cvt_pk_f16_f32 v10, v36, v37
	v_cvt_pk_f16_f32 v11, v38, v39
	s_mov_b32 s0, 0x10000
	ds_write_b128 v208, v[28:31] offset:32768
	ds_write_b128 v209, v[8:11] offset:40960
	v_add_co_u32_e64 v8, s[0:1], s0, v6
	global_load_dwordx4 v[154:157], v[4:5], off offset:272 sc1 nt
	global_load_dwordx4 v[162:165], v[4:5], off offset:256 sc1 nt
	v_addc_co_u32_e64 v9, s[0:1], 0, v7, s[0:1]
	s_mov_b32 s0, 0x12000
	global_load_dwordx4 v[158:161], v[8:9], off sc1
	v_add_co_u32_e64 v8, s[0:1], s0, v6
	v_lshl_add_u32 v211, v12, 6, 0
	s_nop 0
	v_addc_co_u32_e64 v9, s[0:1], 0, v7, s[0:1]
	v_add_co_u32_e64 v10, s[0:1], s34, v6
	v_add_u32_e32 v14, 0x12000, v208
	s_nop 0
	v_addc_co_u32_e64 v11, s[0:1], 0, v7, s[0:1]
	s_mov_b32 s0, 0x16000
	s_nop 0
	v_add_co_u32_e64 v12, s[0:1], s0, v6
	s_waitcnt vmcnt(3)
	ds_write_b128 v14, v[52:55]
	v_addc_co_u32_e64 v13, s[0:1], 0, v7, s[0:1]
	s_mov_b32 s0, 0x18000
	s_nop 0
	v_add_co_u32_e64 v14, s[0:1], s0, v6
	ds_write_b128 v208, v[40:43] offset:49152
	s_nop 0
	v_addc_co_u32_e64 v15, s[0:1], 0, v7, s[0:1]
	s_mov_b32 s0, 0x1a000
	s_nop 0
	v_add_co_u32_e64 v16, s[0:1], s0, v6
	ds_write_b128 v208, v[44:47] offset:57344
	s_nop 0
	v_addc_co_u32_e64 v17, s[0:1], 0, v7, s[0:1]
	s_mov_b32 s0, 0x1c000
	ds_write_b128 v213, v[48:51] offset:57344
	v_add_co_u32_e64 v18, s[0:1], s0, v6
	v_add_u32_e32 v216, v211, v210
	s_nop 0
	v_addc_co_u32_e64 v19, s[0:1], 0, v7, s[0:1]
	global_load_dwordx4 v[174:177], v[8:9], off sc1
	global_load_dwordx4 v[166:169], v[10:11], off sc1
	global_load_dwordx4 v[170:173], v[12:13], off sc1
	global_load_dwordx4 v[142:145], v[4:5], off offset:400 sc1 nt
	global_load_dwordx4 v[150:153], v[4:5], off offset:384 sc1 nt
	global_load_dwordx4 v[138:141], v[14:15], off sc1
	global_load_dwordx4 v[146:149], v[16:17], off sc1
	global_load_dwordx4 v[134:137], v[18:19], off sc1
	s_mov_b32 s0, 0x1e000
	v_add_co_u32_e64 v8, s[0:1], s0, v6
	s_nop 1
	v_addc_co_u32_e64 v9, s[0:1], 0, v7, s[0:1]
	global_load_dwordx4 v[130:133], v[8:9], off sc1
	s_waitcnt lgkmcnt(0)
	s_barrier
	v_lshl_add_u32 v218, v206, 6, 0
	v_add_u32_e32 v217, v218, v210
	ds_read_b128 v[198:201], v216 offset:8192
	ds_read_b128 v[194:197], v216 offset:10240
	ds_read_b128 v[190:193], v216 offset:12288
	ds_read_b128 v[178:181], v216 offset:14336
	ds_read_b128 v[186:189], v217
	ds_read_b128 v[182:185], v217 offset:2048
	v_and_b32_e32 v20, 3, v0
	v_lshl_or_b32 v2, v20, 5, v2
	s_mov_b64 s[0:1], 0x2e000
	v_lshlrev_b32_e32 v212, 4, v1
	v_lshl_add_u64 v[202:203], v[6:7], 0, s[0:1]
	s_mov_b64 s[0:1], 0x290
	v_lshl_add_u64 v[4:5], s[24:25], 0, v[2:3]
	v_lshl_add_u64 v[204:205], v[4:5], 0, s[0:1]
	s_mov_b64 s[24:25], 0x10000
	v_mov_b32_e32 v2, v3
	v_mov_b32_e32 v4, v3
	v_mov_b32_e32 v5, v3
	v_mov_b32_e32 v6, v3
	v_mov_b32_e32 v7, v3
	v_mov_b32_e32 v8, v3
	v_mov_b32_e32 v9, v3
	v_mov_b32_e32 v10, v3
	v_mov_b32_e32 v11, v3
	v_mov_b32_e32 v12, v3
	v_mov_b32_e32 v13, v3
	v_mov_b32_e32 v14, v3
	v_mov_b32_e32 v15, v3
	v_mov_b32_e32 v16, v3
	v_mov_b32_e32 v17, v3
	v_mov_b32_e32 v18, v3
	v_mov_b32_e32 v19, v3
	v_mov_b32_e32 v20, v3
	v_mov_b32_e32 v21, v3
	v_mov_b32_e32 v22, v3
	v_mov_b32_e32 v23, v3
	v_mov_b32_e32 v24, v3
	v_mov_b32_e32 v25, v3
	v_mov_b32_e32 v26, v3
	v_mov_b32_e32 v27, v3
	v_mov_b32_e32 v28, v3
	v_mov_b32_e32 v29, v3
	v_mov_b32_e32 v30, v3
	v_mov_b32_e32 v31, v3
	v_mov_b32_e32 v32, v3
	v_mov_b32_e32 v33, v3
	v_mov_b32_e32 v34, v3
	v_mov_b32_e32 v35, v3
	v_mov_b32_e32 v36, v3
	v_mov_b32_e32 v37, v3
	v_mov_b32_e32 v38, v3
	v_mov_b32_e32 v39, v3
	v_mov_b32_e32 v40, v3
	v_mov_b32_e32 v41, v3
	v_mov_b32_e32 v42, v3
	v_mov_b32_e32 v43, v3
	v_mov_b32_e32 v44, v3
	v_mov_b32_e32 v45, v3
	v_mov_b32_e32 v46, v3
	v_mov_b32_e32 v47, v3
	v_mov_b32_e32 v48, v3
	v_mov_b32_e32 v49, v3
	v_mov_b32_e32 v50, v3
	v_mov_b32_e32 v51, v3
	v_mov_b32_e32 v52, v3
	v_mov_b32_e32 v53, v3
	v_mov_b32_e32 v54, v3
	v_mov_b32_e32 v55, v3
	v_mov_b32_e32 v71, v3
	v_mov_b32_e32 v72, v3
	v_mov_b32_e32 v73, v3
	v_mov_b32_e32 v74, v3
	v_mov_b32_e32 v75, v3
	v_mov_b32_e32 v76, v3
	v_mov_b32_e32 v77, v3
	v_mov_b32_e32 v78, v3
	v_mov_b32_e32 v79, v3
	v_mov_b32_e32 v80, v3
	v_mov_b32_e32 v81, v3
	v_mov_b32_e32 v82, v3
	v_mov_b32_e32 v83, v3
	v_mov_b32_e32 v84, v3
	v_mov_b32_e32 v85, v3
	v_mov_b32_e32 v86, v3
	v_mov_b32_e32 v87, v3
	v_mov_b32_e32 v88, v3
	v_mov_b32_e32 v89, v3
	v_mov_b32_e32 v90, v3
	v_mov_b32_e32 v91, v3
	v_mov_b32_e32 v92, v3
	v_mov_b32_e32 v93, v3
	v_mov_b32_e32 v94, v3
	v_mov_b32_e32 v95, v3
	v_mov_b32_e32 v96, v3
	v_mov_b32_e32 v97, v3
	v_mov_b32_e32 v98, v3
	v_mov_b32_e32 v99, v3
	v_mov_b32_e32 v100, v3
	v_mov_b32_e32 v101, v3
	v_mov_b32_e32 v102, v3
	v_mov_b32_e32 v103, v3
	v_mov_b32_e32 v104, v3
	v_mov_b32_e32 v105, v3
	v_mov_b32_e32 v106, v3
	v_mov_b32_e32 v107, v3
	v_mov_b32_e32 v108, v3
	v_mov_b32_e32 v109, v3
	v_mov_b32_e32 v110, v3
	v_mov_b32_e32 v111, v3
	v_mov_b32_e32 v112, v3
	v_mov_b32_e32 v113, v3
	v_mov_b32_e32 v114, v3
	v_mov_b32_e32 v115, v3
	v_mov_b32_e32 v116, v3
	v_mov_b32_e32 v117, v3
	v_mov_b32_e32 v118, v3
	v_mov_b32_e32 v119, v3
	v_mov_b32_e32 v120, v3
	v_mov_b32_e32 v121, v3
	v_mov_b32_e32 v122, v3
	v_mov_b32_e32 v123, v3
	v_mov_b32_e32 v124, v3
	v_mov_b32_e32 v125, v3
	v_mov_b32_e32 v126, v3
	v_mov_b32_e32 v127, v3
	v_mov_b32_e32 v128, v3
	v_mov_b32_e32 v129, v3
	v_and_b32_e32 v1, 63, v0
	v_add_u32_e32 v215, v211, v212
	v_add_u32_e32 v214, v218, v212
.LBB1_1:
	s_waitcnt lgkmcnt(0)
	v_mfma_f32_32x32x16_f16 v[114:129], v[198:201], v[186:189], v[114:129]
	s_mov_b32 s44, s33
	s_mov_b32 s33, s43
	v_mfma_f32_32x32x16_f16 v[98:113], v[198:201], v[182:185], v[98:113]
	v_add_u32_e32 v219, s33, v215
	ds_read_b128 v[198:201], v219 offset:8192
	ds_read_b128 v[220:223], v219 offset:10240
	ds_read_b128 v[224:227], v219 offset:12288
	ds_read_b128 v[228:231], v219 offset:14336
	v_add_u32_e32 v219, s33, v214
	ds_read_b128 v[232:235], v219
	ds_read_b128 v[236:239], v219 offset:2048
	s_waitcnt vmcnt(10)
	v_cvt_pk_f16_f32 v162, v162, v163
	v_cvt_pk_f16_f32 v163, v164, v165
	v_cvt_pk_f16_f32 v164, v154, v155
	v_cvt_pk_f16_f32 v165, v156, v157
	v_add_u32_e32 v154, s34, v209
	ds_write_b128 v154, v[162:165]
	v_mfma_f32_32x32x16_f16 v[82:97], v[194:197], v[186:189], v[82:97]
	v_add_u32_e32 v154, s34, v208
	s_waitcnt vmcnt(9)
	ds_write_b128 v154, v[158:161] offset:8192
	s_waitcnt vmcnt(8)
	ds_write_b128 v154, v[174:177] offset:16384
	v_mfma_f32_32x32x16_f16 v[66:81], v[194:197], v[182:185], v[66:81]
	v_mfma_f32_32x32x16_f16 v[50:65], v[190:193], v[186:189], v[50:65]
	s_waitcnt vmcnt(7)
	ds_write_b128 v154, v[166:169] offset:24576
	s_waitcnt vmcnt(6)
	ds_write_b128 v154, v[170:173] offset:32768
	v_mfma_f32_32x32x16_f16 v[34:49], v[190:193], v[182:185], v[34:49]
	v_add_co_u32_e64 v158, s[0:1], s36, v202
	global_load_dwordx4 v[154:157], v[204:205], off offset:-128 sc1 nt
	global_load_dwordx4 v[162:165], v[204:205], off offset:-144 sc1 nt
	v_addc_co_u32_e64 v159, s[0:1], -1, v203, s[0:1]
	v_add_co_u32_e64 v166, s[0:1], s37, v202
	v_mfma_f32_32x32x16_f16 v[18:33], v[178:181], v[186:189], v[18:33]
	s_nop 0
	v_addc_co_u32_e64 v167, s[0:1], -1, v203, s[0:1]
	global_load_dwordx4 v[158:161], v[158:159], off sc1
	s_nop 0
	global_load_dwordx4 v[174:177], v[166:167], off sc1
	v_add_co_u32_e64 v166, s[0:1], s38, v202
	s_nop 1
	v_addc_co_u32_e64 v167, s[0:1], -1, v203, s[0:1]
	v_add_co_u32_e64 v170, s[0:1], s39, v202
	v_mfma_f32_32x32x16_f16 v[2:17], v[178:181], v[182:185], v[2:17]
	s_nop 0
	v_addc_co_u32_e64 v171, s[0:1], -1, v203, s[0:1]
	global_load_dwordx4 v[166:169], v[166:167], off sc1
	s_nop 0
	global_load_dwordx4 v[170:173], v[170:171], off sc1
	v_add_u32_e32 v190, s44, v216
	ds_read_b128 v[178:181], v190 offset:8192
	ds_read_b128 v[182:185], v190 offset:10240
	ds_read_b128 v[186:189], v190 offset:12288
	ds_read_b128 v[190:193], v190 offset:14336
	v_add_u32_e32 v219, s44, v217
	ds_read_b128 v[194:197], v219
	ds_read_b128 v[240:243], v219 offset:2048
	s_waitcnt lgkmcnt(12)
	v_mfma_f32_32x32x16_f16 v[114:129], v[198:201], v[232:235], v[114:129]
	s_waitcnt lgkmcnt(11)
	v_mfma_f32_32x32x16_f16 v[98:113], v[198:201], v[236:239], v[98:113]
	v_mfma_f32_32x32x16_f16 v[82:97], v[220:223], v[232:235], v[82:97]
	v_mfma_f32_32x32x16_f16 v[66:81], v[220:223], v[236:239], v[66:81]
	v_mfma_f32_32x32x16_f16 v[50:65], v[224:227], v[232:235], v[50:65]
	v_mfma_f32_32x32x16_f16 v[34:49], v[224:227], v[236:239], v[34:49]
	v_mfma_f32_32x32x16_f16 v[18:33], v[228:231], v[232:235], v[18:33]
	v_mfma_f32_32x32x16_f16 v[2:17], v[228:231], v[236:239], v[2:17]
	s_waitcnt lgkmcnt(1)
	v_mfma_f32_32x32x16_f16 v[114:129], v[178:181], v[194:197], v[114:129]
	s_waitcnt lgkmcnt(0)
	s_barrier
	s_waitcnt lgkmcnt(0)
	v_mfma_f32_32x32x16_f16 v[98:113], v[178:181], v[240:243], v[98:113]
	v_add_u32_e32 v178, s44, v215
	ds_read_b128 v[220:223], v178 offset:8192
	ds_read_b128 v[224:227], v178 offset:10240
	ds_read_b128 v[228:231], v178 offset:12288
	ds_read_b128 v[232:235], v178 offset:14336
	v_add_u32_e32 v178, s44, v214
	ds_read_b128 v[236:239], v178
	ds_read_b128 v[244:247], v178 offset:2048
	s_waitcnt vmcnt(10)
	v_cvt_pk_f16_f32 v150, v150, v151
	v_cvt_pk_f16_f32 v151, v152, v153
	v_cvt_pk_f16_f32 v152, v142, v143
	v_cvt_pk_f16_f32 v153, v144, v145
	v_add_u32_e32 v142, s33, v209
	ds_write_b128 v142, v[150:153]
	v_mfma_f32_32x32x16_f16 v[82:97], v[182:185], v[194:197], v[82:97]
	v_add_u32_e32 v142, s33, v208
	s_waitcnt vmcnt(9)
	ds_write_b128 v142, v[138:141] offset:8192
	s_waitcnt vmcnt(8)
	ds_write_b128 v142, v[146:149] offset:16384
	v_mfma_f32_32x32x16_f16 v[66:81], v[182:185], v[240:243], v[66:81]
	v_mfma_f32_32x32x16_f16 v[50:65], v[186:189], v[194:197], v[50:65]
	s_waitcnt vmcnt(7)
	ds_write_b128 v142, v[134:137] offset:24576
	s_waitcnt vmcnt(6)
	ds_write_b128 v142, v[130:133] offset:32768
	v_mfma_f32_32x32x16_f16 v[34:49], v[186:189], v[240:243], v[34:49]
	v_add_co_u32_e64 v130, s[0:1], s40, v202
	global_load_dwordx4 v[142:145], v[204:205], off sc1 nt
	global_load_dwordx4 v[150:153], v[204:205], off offset:-16 sc1 nt
	v_addc_co_u32_e64 v131, s[0:1], -1, v203, s[0:1]
	v_add_co_u32_e64 v132, s[0:1], s41, v202
	v_mfma_f32_32x32x16_f16 v[18:33], v[190:193], v[194:197], v[18:33]
	s_nop 0
	v_addc_co_u32_e64 v133, s[0:1], -1, v203, s[0:1]
	global_load_dwordx4 v[138:141], v[130:131], off sc1
	global_load_dwordx4 v[146:149], v[132:133], off sc1
	v_add_co_u32_e64 v130, s[0:1], s42, v202
	s_nop 1
	v_addc_co_u32_e64 v131, s[0:1], -1, v203, s[0:1]
	global_load_dwordx4 v[134:137], v[130:131], off sc1
	s_nop 0
	global_load_dwordx4 v[130:133], v[202:203], off sc1
	v_mfma_f32_32x32x16_f16 v[2:17], v[190:193], v[240:243], v[2:17]
	v_add_u32_e32 v178, s34, v216
	ds_read_b128 v[198:201], v178 offset:8192
	ds_read_b128 v[194:197], v178 offset:10240
	ds_read_b128 v[190:193], v178 offset:12288
	ds_read_b128 v[178:181], v178 offset:14336
	v_add_u32_e32 v182, s34, v217
	ds_read_b128 v[186:189], v182
	ds_read_b128 v[182:185], v182 offset:2048
	s_waitcnt lgkmcnt(12)
	v_mfma_f32_32x32x16_f16 v[114:129], v[220:223], v[236:239], v[114:129]
	s_waitcnt lgkmcnt(11)
	v_mfma_f32_32x32x16_f16 v[98:113], v[220:223], v[244:247], v[98:113]
	v_mfma_f32_32x32x16_f16 v[82:97], v[224:227], v[236:239], v[82:97]
	v_mfma_f32_32x32x16_f16 v[66:81], v[224:227], v[244:247], v[66:81]
	v_mfma_f32_32x32x16_f16 v[50:65], v[228:231], v[236:239], v[50:65]
	v_mfma_f32_32x32x16_f16 v[34:49], v[228:231], v[244:247], v[34:49]
	v_mfma_f32_32x32x16_f16 v[18:33], v[232:235], v[236:239], v[18:33]
	v_mfma_f32_32x32x16_f16 v[2:17], v[232:235], v[244:247], v[2:17]
	s_waitcnt lgkmcnt(0)
	s_barrier
	s_add_i32 s35, s35, 2
	v_lshl_add_u64 v[202:203], v[202:203], 0, s[24:25]
	v_lshl_add_u64 v[204:205], v[204:205], 0, s[26:27]
	s_mov_b32 s43, s34
	s_cmp_gt_u32 s35, 9
	s_mov_b32 s34, s44
	s_cbranch_scc0 .LBB1_1
	s_and_b64 s[0:1], s[20:21], exec
	s_cselect_b32 s6, s6, s8
	s_cselect_b32 s7, s7, s9
	s_and_b64 s[0:1], vcc, exec
	s_cselect_b32 s1, s5, s7
	s_cselect_b32 s0, s4, s6
	v_mov_b32_e32 v202, 0x3e38aa3b
	s_waitcnt lgkmcnt(1)
	v_mfma_f32_32x32x16_f16 v[114:129], v[198:201], v[186:189], v[114:129]
	v_cndmask_b32_e32 v202, 1.0, v202, vcc
	s_waitcnt lgkmcnt(0)
	v_mfma_f32_32x32x16_f16 v[98:113], v[198:201], v[182:185], v[98:113]
	ds_read_b128 v[198:201], v215 offset:8192
	ds_read_b128 v[220:223], v215 offset:10240
	ds_read_b128 v[224:227], v215 offset:12288
	ds_read_b128 v[228:231], v215 offset:14336
	ds_read_b128 v[232:235], v214
	ds_read_b128 v[236:239], v214 offset:2048
	s_waitcnt vmcnt(10)
	v_cvt_pk_f16_f32 v162, v162, v163
	v_cvt_pk_f16_f32 v163, v164, v165
	v_cvt_pk_f16_f32 v164, v154, v155
	v_cvt_pk_f16_f32 v165, v156, v157
	v_add_u32_e32 v154, 0x14000, v209
	ds_write_b128 v154, v[162:165]
	v_add_u32_e32 v154, 0x14000, v213
	s_waitcnt vmcnt(9)
	ds_write_b128 v154, v[158:161]
	v_add_u32_e32 v154, 0x16000, v213
	v_mfma_f32_32x32x16_f16 v[82:97], v[194:197], v[186:189], v[82:97]
	s_waitcnt vmcnt(8)
	ds_write_b128 v154, v[174:177]
	v_mfma_f32_32x32x16_f16 v[66:81], v[194:197], v[182:185], v[66:81]
	v_add_u32_e32 v154, 0x18000, v213
	s_waitcnt vmcnt(7)
	ds_write_b128 v154, v[166:169]
	v_add_u32_e32 v154, 0x1a000, v213
	v_mfma_f32_32x32x16_f16 v[50:65], v[190:193], v[186:189], v[50:65]
	s_waitcnt vmcnt(6)
	ds_write_b128 v154, v[170:173]
	v_mfma_f32_32x32x16_f16 v[34:49], v[190:193], v[182:185], v[34:49]
	v_mfma_f32_32x32x16_f16 v[18:33], v[178:181], v[186:189], v[18:33]
	v_mfma_f32_32x32x16_f16 v[2:17], v[178:181], v[182:185], v[2:17]
	ds_read_b128 v[154:157], v216 offset:49152
	ds_read_b128 v[158:161], v216 offset:51200
	ds_read_b128 v[162:165], v216 offset:53248
	ds_read_b128 v[166:169], v216 offset:55296
	ds_read_b128 v[170:173], v217 offset:40960
	ds_read_b128 v[174:177], v217 offset:43008
	s_waitcnt lgkmcnt(12)
	v_mfma_f32_32x32x16_f16 v[114:129], v[198:201], v[232:235], v[114:129]
	s_waitcnt lgkmcnt(11)
	v_mfma_f32_32x32x16_f16 v[98:113], v[198:201], v[236:239], v[98:113]
	v_mfma_f32_32x32x16_f16 v[82:97], v[220:223], v[232:235], v[82:97]
	v_mfma_f32_32x32x16_f16 v[66:81], v[220:223], v[236:239], v[66:81]
	v_mfma_f32_32x32x16_f16 v[50:65], v[224:227], v[232:235], v[50:65]
	v_mfma_f32_32x32x16_f16 v[34:49], v[224:227], v[236:239], v[34:49]
	v_mfma_f32_32x32x16_f16 v[18:33], v[228:231], v[232:235], v[18:33]
	v_mfma_f32_32x32x16_f16 v[2:17], v[228:231], v[236:239], v[2:17]
	s_waitcnt lgkmcnt(0)
	s_barrier
	s_waitcnt lgkmcnt(1)
	v_mfma_f32_32x32x16_f16 v[114:129], v[154:157], v[170:173], v[114:129]
	s_waitcnt lgkmcnt(0)
	v_mfma_f32_32x32x16_f16 v[98:113], v[154:157], v[174:177], v[98:113]
	ds_read_b128 v[154:157], v215 offset:49152
	ds_read_b128 v[178:181], v215 offset:51200
	ds_read_b128 v[182:185], v215 offset:53248
	ds_read_b128 v[186:189], v215 offset:55296
	ds_read_b128 v[190:193], v214 offset:40960
	ds_read_b128 v[194:197], v214 offset:43008
	s_waitcnt vmcnt(4)
	v_cvt_pk_f16_f32 v150, v150, v151
	v_cvt_pk_f16_f32 v151, v152, v153
	v_cvt_pk_f16_f32 v152, v142, v143
	v_cvt_pk_f16_f32 v153, v144, v145
	ds_write_b128 v209, v[150:153]
	v_mfma_f32_32x32x16_f16 v[82:97], v[158:161], v[170:173], v[82:97]
	s_waitcnt vmcnt(3)
	ds_write_b128 v208, v[138:141] offset:8192
	s_waitcnt vmcnt(2)
	ds_write_b128 v208, v[146:149] offset:16384
	v_mfma_f32_32x32x16_f16 v[66:81], v[158:161], v[174:177], v[66:81]
	v_mfma_f32_32x32x16_f16 v[50:65], v[162:165], v[170:173], v[50:65]
	s_waitcnt vmcnt(1)
	ds_write_b128 v208, v[134:137] offset:24576
	s_waitcnt vmcnt(0)
	ds_write_b128 v208, v[130:133] offset:32768
	v_mfma_f32_32x32x16_f16 v[34:49], v[162:165], v[174:177], v[34:49]
	v_mfma_f32_32x32x16_f16 v[18:33], v[166:169], v[170:173], v[18:33]
	v_mfma_f32_32x32x16_f16 v[2:17], v[166:169], v[174:177], v[2:17]
	v_add_u32_e32 v158, 0x16000, v211
	v_add_u32_e32 v142, v158, v210
	ds_read_b128 v[130:133], v142
	ds_read_b128 v[134:137], v142 offset:2048
	ds_read_b128 v[138:141], v142 offset:4096
	ds_read_b128 v[142:145], v142 offset:6144
	v_add_u32_e32 v166, 0x14000, v218
	v_add_u32_e32 v150, v166, v210
	ds_read_b128 v[146:149], v150
	ds_read_b128 v[150:153], v150 offset:2048
	s_waitcnt lgkmcnt(12)
	v_mfma_f32_32x32x16_f16 v[114:129], v[154:157], v[190:193], v[114:129]
	s_waitcnt lgkmcnt(11)
	v_mfma_f32_32x32x16_f16 v[98:113], v[154:157], v[194:197], v[98:113]
	v_mfma_f32_32x32x16_f16 v[82:97], v[178:181], v[190:193], v[82:97]
	v_mfma_f32_32x32x16_f16 v[66:81], v[178:181], v[194:197], v[66:81]
	v_mfma_f32_32x32x16_f16 v[50:65], v[182:185], v[190:193], v[50:65]
	v_mfma_f32_32x32x16_f16 v[34:49], v[182:185], v[194:197], v[34:49]
	v_mfma_f32_32x32x16_f16 v[18:33], v[186:189], v[190:193], v[18:33]
	v_mfma_f32_32x32x16_f16 v[2:17], v[186:189], v[194:197], v[2:17]
	s_waitcnt lgkmcnt(0)
	s_barrier
	s_waitcnt lgkmcnt(1)
	v_mfma_f32_32x32x16_f16 v[114:129], v[130:133], v[146:149], v[114:129]
	s_waitcnt lgkmcnt(0)
	v_mfma_f32_32x32x16_f16 v[98:113], v[130:133], v[150:153], v[98:113]
	v_add_u32_e32 v162, v158, v212
	ds_read_b128 v[130:133], v162
	ds_read_b128 v[154:157], v162 offset:2048
	ds_read_b128 v[158:161], v162 offset:4096
	ds_read_b128 v[162:165], v162 offset:6144
	v_add_u32_e32 v170, v166, v212
	ds_read_b128 v[166:169], v170
	ds_read_b128 v[170:173], v170 offset:2048
	v_mfma_f32_32x32x16_f16 v[82:97], v[134:137], v[146:149], v[82:97]
	v_mfma_f32_32x32x16_f16 v[66:81], v[134:137], v[150:153], v[66:81]
	v_mfma_f32_32x32x16_f16 v[50:65], v[138:141], v[146:149], v[50:65]
	v_mfma_f32_32x32x16_f16 v[34:49], v[138:141], v[150:153], v[34:49]
	v_mfma_f32_32x32x16_f16 v[18:33], v[142:145], v[146:149], v[18:33]
	v_mfma_f32_32x32x16_f16 v[2:17], v[142:145], v[150:153], v[2:17]
	ds_read_b128 v[134:137], v216 offset:8192
	ds_read_b128 v[138:141], v216 offset:10240
	ds_read_b128 v[142:145], v216 offset:12288
	ds_read_b128 v[146:149], v216 offset:14336
	ds_read_b128 v[150:153], v217
	ds_read_b128 v[174:177], v217 offset:2048
	s_waitcnt lgkmcnt(7)
	v_mfma_f32_32x32x16_f16 v[114:129], v[130:133], v[166:169], v[114:129]
	s_waitcnt lgkmcnt(6)
	v_mfma_f32_32x32x16_f16 v[98:113], v[130:133], v[170:173], v[98:113]
	v_mfma_f32_32x32x16_f16 v[82:97], v[154:157], v[166:169], v[82:97]
	v_mfma_f32_32x32x16_f16 v[66:81], v[154:157], v[170:173], v[66:81]
	v_mfma_f32_32x32x16_f16 v[50:65], v[158:161], v[166:169], v[50:65]
	v_mfma_f32_32x32x16_f16 v[34:49], v[158:161], v[170:173], v[34:49]
	v_mfma_f32_32x32x16_f16 v[18:33], v[162:165], v[166:169], v[18:33]
	v_mfma_f32_32x32x16_f16 v[2:17], v[162:165], v[170:173], v[2:17]
	s_waitcnt lgkmcnt(0)
	s_barrier
	s_waitcnt lgkmcnt(1)
	v_mfma_f32_32x32x16_f16 v[114:129], v[134:137], v[150:153], v[114:129]
	s_waitcnt lgkmcnt(0)
	v_mfma_f32_32x32x16_f16 v[98:113], v[134:137], v[174:177], v[98:113]
	ds_read_b128 v[130:133], v215 offset:8192
	ds_read_b128 v[134:137], v215 offset:10240
	ds_read_b128 v[154:157], v215 offset:12288
	ds_read_b128 v[158:161], v215 offset:14336
	ds_read_b128 v[162:165], v214
	ds_read_b128 v[166:169], v214 offset:2048
	v_mfma_f32_32x32x16_f16 v[82:97], v[138:141], v[150:153], v[82:97]
	v_mfma_f32_32x32x16_f16 v[66:81], v[138:141], v[174:177], v[66:81]
	v_mfma_f32_32x32x16_f16 v[50:65], v[142:145], v[150:153], v[50:65]
	v_mfma_f32_32x32x16_f16 v[34:49], v[142:145], v[174:177], v[34:49]
	v_mfma_f32_32x32x16_f16 v[18:33], v[146:149], v[150:153], v[18:33]
	v_mfma_f32_32x32x16_f16 v[2:17], v[146:149], v[174:177], v[2:17]
	s_waitcnt lgkmcnt(1)
	v_mfma_f32_32x32x16_f16 v[114:129], v[130:133], v[162:165], v[114:129]
	s_waitcnt lgkmcnt(0)
	v_mfma_f32_32x32x16_f16 v[98:113], v[130:133], v[166:169], v[98:113]
	v_mfma_f32_32x32x16_f16 v[82:97], v[134:137], v[162:165], v[82:97]
	v_mfma_f32_32x32x16_f16 v[66:81], v[134:137], v[166:169], v[66:81]
	v_mfma_f32_32x32x16_f16 v[50:65], v[154:157], v[162:165], v[50:65]
	v_mfma_f32_32x32x16_f16 v[34:49], v[154:157], v[166:169], v[34:49]
	v_mfma_f32_32x32x16_f16 v[18:33], v[158:161], v[162:165], v[18:33]
	v_mfma_f32_32x32x16_f16 v[2:17], v[158:161], v[166:169], v[2:17]
	v_lshl_or_b32 v130, v207, 2, s31
	s_waitcnt lgkmcnt(0)
	s_barrier
	v_lshlrev_b32_e32 v154, 2, v130
	global_load_dwordx4 v[134:137], v154, s[0:1]
	global_load_dwordx4 v[150:153], v154, s[0:1] offset:32
	global_load_dwordx4 v[156:159], v154, s[0:1] offset:64
	global_load_dwordx4 v[160:163], v154, s[0:1] offset:96
	global_load_dwordx4 v[164:167], v154, s[0:1] offset:128
	global_load_dwordx4 v[168:171], v154, s[0:1] offset:160
	s_movk_i32 s4, 0x410
	v_lshlrev_b32_e32 v130, 1, v130
	v_mul_lo_u32 v131, v206, s4
	v_add3_u32 v155, 0, v130, v131
	global_load_dwordx4 v[172:175], v154, s[0:1] offset:192
	global_load_dwordx4 v[146:149], v154, s[0:1] offset:224
	global_load_dwordx4 v[142:145], v154, s[0:1] offset:256
	global_load_dwordx4 v[130:133], v154, s[0:1] offset:288
	global_load_dwordx4 v[138:141], v154, s[0:1] offset:320
	v_add_u32_e32 v176, 0x8000, v155
	s_waitcnt vmcnt(10)
	v_pk_add_f32 v[114:115], v[134:135], v[114:115]
	v_pk_add_f32 v[116:117], v[136:137], v[116:117]
	v_pk_add_f32 v[98:99], v[134:135], v[98:99]
	v_pk_add_f32 v[100:101], v[136:137], v[100:101]
	s_waitcnt vmcnt(9)
	v_pk_add_f32 v[118:119], v[150:151], v[118:119]
	v_pk_add_f32 v[120:121], v[152:153], v[120:121]
	s_waitcnt vmcnt(6)
	v_pk_add_f32 v[82:83], v[164:165], v[82:83]
	v_pk_add_f32 v[84:85], v[166:167], v[84:85]
	v_pk_add_f32 v[66:67], v[164:165], v[66:67]
	v_pk_add_f32 v[68:69], v[166:167], v[68:69]
	s_waitcnt vmcnt(5)
	v_pk_add_f32 v[70:71], v[168:169], v[70:71]
	v_pk_add_f32 v[72:73], v[170:171], v[72:73]
	v_pk_add_f32 v[102:103], v[150:151], v[102:103]
	v_pk_add_f32 v[104:105], v[152:153], v[104:105]
	v_pk_add_f32 v[122:123], v[156:157], v[122:123]
	v_pk_add_f32 v[124:125], v[158:159], v[124:125]
	v_pk_add_f32 v[106:107], v[156:157], v[106:107]
	v_pk_add_f32 v[108:109], v[158:159], v[108:109]
	v_pk_add_f32 v[126:127], v[160:161], v[126:127]
	v_pk_add_f32 v[128:129], v[162:163], v[128:129]
	v_pk_add_f32 v[110:111], v[160:161], v[110:111]
	v_pk_add_f32 v[112:113], v[162:163], v[112:113]
	v_pk_add_f32 v[86:87], v[168:169], v[86:87]
	v_pk_mul_f32 v[114:115], v[202:203], v[114:115] op_sel_hi:[0,1]
	v_pk_mul_f32 v[116:117], v[202:203], v[116:117] op_sel_hi:[0,1]
	v_pk_mul_f32 v[98:99], v[202:203], v[98:99] op_sel_hi:[0,1]
	v_pk_mul_f32 v[100:101], v[202:203], v[100:101] op_sel_hi:[0,1]
	v_pk_mul_f32 v[118:119], v[202:203], v[118:119] op_sel_hi:[0,1]
	v_pk_mul_f32 v[120:121], v[202:203], v[120:121] op_sel_hi:[0,1]
	v_pk_mul_f32 v[82:83], v[202:203], v[82:83] op_sel_hi:[0,1]
	v_pk_mul_f32 v[84:85], v[202:203], v[84:85] op_sel_hi:[0,1]
	v_pk_mul_f32 v[66:67], v[202:203], v[66:67] op_sel_hi:[0,1]
	v_pk_mul_f32 v[68:69], v[202:203], v[68:69] op_sel_hi:[0,1]
	v_pk_add_f32 v[88:89], v[170:171], v[88:89]
	v_pk_mul_f32 v[70:71], v[202:203], v[70:71] op_sel_hi:[0,1]
	v_pk_mul_f32 v[72:73], v[202:203], v[72:73] op_sel_hi:[0,1]
	v_pk_mul_f32 v[102:103], v[202:203], v[102:103] op_sel_hi:[0,1]
	v_pk_mul_f32 v[104:105], v[202:203], v[104:105] op_sel_hi:[0,1]
	v_pk_mul_f32 v[122:123], v[202:203], v[122:123] op_sel_hi:[0,1]
	v_pk_mul_f32 v[124:125], v[202:203], v[124:125] op_sel_hi:[0,1]
	v_pk_mul_f32 v[106:107], v[202:203], v[106:107] op_sel_hi:[0,1]
	v_pk_mul_f32 v[108:109], v[202:203], v[108:109] op_sel_hi:[0,1]
	v_pk_mul_f32 v[126:127], v[202:203], v[126:127] op_sel_hi:[0,1]
	v_pk_mul_f32 v[128:129], v[202:203], v[128:129] op_sel_hi:[0,1]
	v_pk_mul_f32 v[110:111], v[202:203], v[110:111] op_sel_hi:[0,1]
	v_pk_mul_f32 v[112:113], v[202:203], v[112:113] op_sel_hi:[0,1]
	v_pk_mul_f32 v[86:87], v[202:203], v[86:87] op_sel_hi:[0,1]
	v_cvt_pk_f16_f32 v114, v114, v115
	v_cvt_pk_f16_f32 v115, v116, v117
	v_cvt_pk_f16_f32 v98, v98, v99
	v_cvt_pk_f16_f32 v99, v100, v101
	v_cvt_pk_f16_f32 v100, v118, v119
	v_cvt_pk_f16_f32 v101, v120, v121
	v_cvt_pk_f16_f32 v82, v82, v83
	v_cvt_pk_f16_f32 v83, v84, v85
	v_cvt_pk_f16_f32 v84, v66, v67
	v_cvt_pk_f16_f32 v85, v68, v69
	v_pk_mul_f32 v[88:89], v[202:203], v[88:89] op_sel_hi:[0,1]
	v_cvt_pk_f16_f32 v70, v70, v71
	v_cvt_pk_f16_f32 v71, v72, v73
	v_cvt_pk_f16_f32 v102, v102, v103
	v_cvt_pk_f16_f32 v103, v104, v105
	v_cvt_pk_f16_f32 v104, v122, v123
	v_cvt_pk_f16_f32 v105, v124, v125
	v_cvt_pk_f16_f32 v106, v106, v107
	v_cvt_pk_f16_f32 v107, v108, v109
	v_cvt_pk_f16_f32 v108, v126, v127
	v_cvt_pk_f16_f32 v109, v128, v129
	v_cvt_pk_f16_f32 v110, v110, v111
	v_cvt_pk_f16_f32 v111, v112, v113
	v_cvt_pk_f16_f32 v86, v86, v87
	ds_write2_b64 v155, v[114:115], v[100:101] offset1:2
	ds_write2_b64 v176, v[98:99], v[102:103] offset0:64 offset1:66
	ds_write2_b64 v155, v[104:105], v[108:109] offset0:4 offset1:6
	ds_write2_b64 v176, v[106:107], v[110:111] offset0:68 offset1:70
	v_cvt_pk_f16_f32 v87, v88, v89
	ds_write2_b64 v176, v[84:85], v[70:71] offset0:72 offset1:74
	s_waitcnt vmcnt(4)
	v_pk_add_f32 v[70:71], v[172:173], v[90:91]
	v_pk_add_f32 v[84:85], v[174:175], v[92:93]
	v_pk_add_f32 v[74:75], v[172:173], v[74:75]
	ds_write2_b64 v155, v[82:83], v[86:87] offset0:8 offset1:10
	v_pk_mul_f32 v[82:83], v[202:203], v[70:71] op_sel_hi:[0,1]
	v_pk_mul_f32 v[84:85], v[202:203], v[84:85] op_sel_hi:[0,1]
	v_pk_mul_f32 v[74:75], v[202:203], v[74:75] op_sel_hi:[0,1]
	global_load_dwordx4 v[66:69], v154, s[0:1] offset:352
	global_load_dwordx4 v[70:73], v154, s[0:1] offset:384
	v_cvt_pk_f16_f32 v82, v82, v83
	v_cvt_pk_f16_f32 v83, v84, v85
	v_cvt_pk_f16_f32 v84, v74, v75
	v_pk_add_f32 v[74:75], v[174:175], v[76:77]
	s_waitcnt vmcnt(5)
	v_pk_add_f32 v[78:79], v[146:147], v[78:79]
	v_pk_mul_f32 v[74:75], v[202:203], v[74:75] op_sel_hi:[0,1]
	v_cvt_pk_f16_f32 v85, v74, v75
	global_load_dwordx4 v[74:77], v154, s[0:1] offset:416
	v_pk_add_f32 v[80:81], v[148:149], v[80:81]
	v_pk_mul_f32 v[78:79], v[202:203], v[78:79] op_sel_hi:[0,1]
	v_pk_mul_f32 v[80:81], v[202:203], v[80:81] op_sel_hi:[0,1]
	v_cvt_pk_f16_f32 v78, v78, v79
	v_cvt_pk_f16_f32 v79, v80, v81
	ds_write2_b64 v176, v[84:85], v[78:79] offset0:76 offset1:78
	global_load_dwordx4 v[78:81], v154, s[0:1] offset:448
	v_pk_add_f32 v[86:87], v[146:147], v[94:95]
	v_pk_add_f32 v[88:89], v[148:149], v[96:97]
	s_waitcnt vmcnt(6)
	v_pk_add_f32 v[50:51], v[142:143], v[50:51]
	v_pk_add_f32 v[52:53], v[144:145], v[52:53]
	v_pk_add_f32 v[34:35], v[142:143], v[34:35]
	v_pk_mul_f32 v[86:87], v[202:203], v[86:87] op_sel_hi:[0,1]
	v_pk_mul_f32 v[88:89], v[202:203], v[88:89] op_sel_hi:[0,1]
	v_pk_mul_f32 v[50:51], v[202:203], v[50:51] op_sel_hi:[0,1]
	v_pk_mul_f32 v[52:53], v[202:203], v[52:53] op_sel_hi:[0,1]
	v_pk_mul_f32 v[34:35], v[202:203], v[34:35] op_sel_hi:[0,1]
	v_cvt_pk_f16_f32 v86, v86, v87
	v_cvt_pk_f16_f32 v87, v88, v89
	v_cvt_pk_f16_f32 v50, v50, v51
	v_cvt_pk_f16_f32 v51, v52, v53
	v_cvt_pk_f16_f32 v52, v34, v35
	v_pk_add_f32 v[34:35], v[144:145], v[36:37]
	ds_write2_b64 v155, v[82:83], v[86:87] offset0:12 offset1:14
	v_pk_mul_f32 v[82:83], v[202:203], v[34:35] op_sel_hi:[0,1]
	global_load_dwordx4 v[34:37], v154, s[0:1] offset:480
	s_waitcnt vmcnt(6)
	v_pk_add_f32 v[38:39], v[130:131], v[38:39]
	v_pk_add_f32 v[40:41], v[132:133], v[40:41]
	v_pk_mul_f32 v[38:39], v[202:203], v[38:39] op_sel_hi:[0,1]
	v_pk_mul_f32 v[40:41], v[202:203], v[40:41] op_sel_hi:[0,1]
	v_cvt_pk_f16_f32 v53, v82, v83
	v_cvt_pk_f16_f32 v38, v38, v39
	v_cvt_pk_f16_f32 v39, v40, v41
	ds_write2_b64 v176, v[52:53], v[38:39] offset0:80 offset1:82
	s_waitcnt vmcnt(5)
	v_pk_add_f32 v[38:39], v[138:139], v[58:59]
	v_pk_add_f32 v[40:41], v[140:141], v[60:61]
	v_pk_mul_f32 v[38:39], v[202:203], v[38:39] op_sel_hi:[0,1]
	v_pk_mul_f32 v[40:41], v[202:203], v[40:41] op_sel_hi:[0,1]
	v_cvt_pk_f16_f32 v38, v38, v39
	v_cvt_pk_f16_f32 v39, v40, v41
	v_pk_add_f32 v[40:41], v[138:139], v[42:43]
	v_pk_add_f32 v[42:43], v[140:141], v[44:45]
	v_pk_mul_f32 v[40:41], v[202:203], v[40:41] op_sel_hi:[0,1]
	v_pk_mul_f32 v[42:43], v[202:203], v[42:43] op_sel_hi:[0,1]
	v_cvt_pk_f16_f32 v40, v40, v41
	v_cvt_pk_f16_f32 v41, v42, v43
	v_pk_add_f32 v[54:55], v[130:131], v[54:55]
	v_pk_add_f32 v[56:57], v[132:133], v[56:57]
	v_pk_mul_f32 v[54:55], v[202:203], v[54:55] op_sel_hi:[0,1]
	v_pk_mul_f32 v[56:57], v[202:203], v[56:57] op_sel_hi:[0,1]
	v_cmp_gt_u32_e64 s[0:1], 8, v0
	v_cvt_pk_f16_f32 v54, v54, v55
	v_cvt_pk_f16_f32 v55, v56, v57
	s_and_b64 s[6:7], s[20:21], s[0:1]
	ds_write2_b64 v155, v[50:51], v[54:55] offset0:16 offset1:18
	s_waitcnt vmcnt(4)
	v_pk_add_f32 v[42:43], v[66:67], v[62:63]
	s_waitcnt vmcnt(3)
	v_pk_add_f32 v[18:19], v[70:71], v[18:19]
	v_pk_add_f32 v[20:21], v[72:73], v[20:21]
	v_pk_add_f32 v[2:3], v[70:71], v[2:3]
	v_pk_add_f32 v[4:5], v[72:73], v[4:5]
	v_pk_mul_f32 v[18:19], v[202:203], v[18:19] op_sel_hi:[0,1]
	v_pk_mul_f32 v[20:21], v[202:203], v[20:21] op_sel_hi:[0,1]
	v_pk_mul_f32 v[2:3], v[202:203], v[2:3] op_sel_hi:[0,1]
	v_pk_mul_f32 v[4:5], v[202:203], v[4:5] op_sel_hi:[0,1]
	v_cvt_pk_f16_f32 v18, v18, v19
	v_cvt_pk_f16_f32 v19, v20, v21
	v_cvt_pk_f16_f32 v2, v2, v3
	v_cvt_pk_f16_f32 v3, v4, v5
	s_waitcnt vmcnt(2)
	v_pk_add_f32 v[4:5], v[74:75], v[22:23]
	v_pk_add_f32 v[20:21], v[76:77], v[24:25]
	v_pk_mul_f32 v[4:5], v[202:203], v[4:5] op_sel_hi:[0,1]
	v_pk_mul_f32 v[20:21], v[202:203], v[20:21] op_sel_hi:[0,1]
	v_cvt_pk_f16_f32 v4, v4, v5
	v_cvt_pk_f16_f32 v5, v20, v21
	ds_write2_b64 v155, v[18:19], v[4:5] offset0:24 offset1:26
	v_pk_add_f32 v[4:5], v[74:75], v[6:7]
	v_pk_add_f32 v[6:7], v[76:77], v[8:9]
	v_pk_mul_f32 v[4:5], v[202:203], v[4:5] op_sel_hi:[0,1]
	v_pk_mul_f32 v[6:7], v[202:203], v[6:7] op_sel_hi:[0,1]
	v_cvt_pk_f16_f32 v4, v4, v5
	v_cvt_pk_f16_f32 v5, v6, v7
	ds_write2_b64 v176, v[2:3], v[4:5] offset0:88 offset1:90
	s_waitcnt vmcnt(1)
	v_pk_add_f32 v[2:3], v[78:79], v[26:27]
	v_pk_add_f32 v[4:5], v[80:81], v[28:29]
	v_pk_mul_f32 v[2:3], v[202:203], v[2:3] op_sel_hi:[0,1]
	v_pk_mul_f32 v[4:5], v[202:203], v[4:5] op_sel_hi:[0,1]
	v_cvt_pk_f16_f32 v2, v2, v3
	v_cvt_pk_f16_f32 v3, v4, v5
	v_pk_add_f32 v[4:5], v[78:79], v[10:11]
	v_pk_add_f32 v[6:7], v[80:81], v[12:13]
	v_pk_mul_f32 v[4:5], v[202:203], v[4:5] op_sel_hi:[0,1]
	v_pk_mul_f32 v[6:7], v[202:203], v[6:7] op_sel_hi:[0,1]
	v_pk_add_f32 v[44:45], v[68:69], v[64:65]
	v_cvt_pk_f16_f32 v4, v4, v5
	v_cvt_pk_f16_f32 v5, v6, v7
	s_waitcnt vmcnt(0)
	v_pk_add_f32 v[6:7], v[34:35], v[30:31]
	v_pk_add_f32 v[8:9], v[36:37], v[32:33]
	v_pk_mul_f32 v[42:43], v[202:203], v[42:43] op_sel_hi:[0,1]
	v_pk_mul_f32 v[44:45], v[202:203], v[44:45] op_sel_hi:[0,1]
	v_pk_mul_f32 v[6:7], v[202:203], v[6:7] op_sel_hi:[0,1]
	v_pk_mul_f32 v[8:9], v[202:203], v[8:9] op_sel_hi:[0,1]
	v_cvt_pk_f16_f32 v42, v42, v43
	v_cvt_pk_f16_f32 v43, v44, v45
	v_cvt_pk_f16_f32 v6, v6, v7
	v_cvt_pk_f16_f32 v7, v8, v9
	ds_write2_b64 v155, v[38:39], v[42:43] offset0:20 offset1:22
	v_pk_add_f32 v[38:39], v[66:67], v[46:47]
	v_pk_add_f32 v[42:43], v[68:69], v[48:49]
	ds_write2_b64 v155, v[2:3], v[6:7] offset0:28 offset1:30
	v_pk_add_f32 v[2:3], v[34:35], v[14:15]
	v_pk_add_f32 v[6:7], v[36:37], v[16:17]
	v_pk_mul_f32 v[38:39], v[202:203], v[38:39] op_sel_hi:[0,1]
	v_pk_mul_f32 v[42:43], v[202:203], v[42:43] op_sel_hi:[0,1]
	v_pk_mul_f32 v[2:3], v[202:203], v[2:3] op_sel_hi:[0,1]
	v_pk_mul_f32 v[6:7], v[202:203], v[6:7] op_sel_hi:[0,1]
	v_cvt_pk_f16_f32 v38, v38, v39
	v_cvt_pk_f16_f32 v39, v42, v43
	v_cvt_pk_f16_f32 v2, v2, v3
	v_cvt_pk_f16_f32 v3, v6, v7
	ds_write2_b64 v176, v[40:41], v[38:39] offset0:84 offset1:86
	ds_write2_b64 v176, v[4:5], v[2:3] offset0:92 offset1:94
	s_and_saveexec_b64 s[4:5], s[6:7]
	v_lshl_add_u32 v2, v0, 2, 0
	v_add_u32_e32 v2, 0x20800, v2
	v_mov_b32_e32 v3, 0
	ds_write_b32 v2, v3
	s_or_b64 exec, exec, s[4:5]
	s_waitcnt lgkmcnt(0)
	s_barrier
	s_mov_b64 s[4:5], -1
	s_and_b64 vcc, exec, s[22:23]
	s_cbranch_vccnz .LBB1_7
	s_andn2_b64 vcc, exec, s[4:5]
	s_cbranch_vccz .LBB1_14
